# phase pin (docs 9.3): the seven GEMM K-loop heads aligned to 64 bytes (.p2align 6), on top of one priority raise per MFMA segment
# baseline (speedup 1.0000x reference)
; template <class Epi, class Sched, bool ALIGN_EPI = false, bool SP2 = false>
; __device__ __forceinline__ void gemm_phase(PG8_LAS unsigned char* lds, const Gemm g, const Sched& S, const Epi& E) {
;     ...
;         const bool has_next = S.next(ui + 1, nxt);
;         const char* nA = has_next ? (const char*)g.A + (size_t)nxt.pm * tstep : cA; const char* nB = has_next ? (const char*)g.Bt + (size_t)nxt.pn * tstep : cB;
;         for (int t = 0; t < nt; t += 2) {
;             if constexpr (Epi::MIDK) { if (t == (nt >> 1)) E.mid(acc, cur, wr, wc, fr, fq); }
;             const bool last = (t == nt - 2);
;             const char* a1 = cA + (size_t)(t + 1) * kstep;
;             const char* a2 = last ? nA : cA + (size_t)(t + 2) * kstep; const char* b2 = last ? nB : cB + (size_t)(t + 2) * kstep;
;             const char* a3 = a2 + kstep; const char* b3 = b2 + kstep;
;     ...
; #pragma unroll
;         for (int a = 0; a < 2; ++a)
; #pragma unroll
;             for (int b = 0; b < 2; ++b)
; #pragma unroll
;                 for (int m = 0; m < 4; ++m)
; #pragma unroll
;                     for (int n = 0; n < 2; ++n) acc[a][b][m][n] = (f32x4){0.f, 0.f, 0.f, 0.f};
;         cur = nxt; cA = nA; cB = nB; ++ui;
.Lzk_1:
	s_add_u32 s2, s50, 0x80
	s_addc_u32 s3, s51, 0
	s_add_u32 s20, s48, 0x100
	s_addc_u32 s52, s49, 0
	s_mov_b32 s48, 0
	v_mov_b64_e32 v[42:43], 0
	v_mov_b64_e32 v[44:45], 0
	v_mov_b64_e32 v[46:47], 0
	v_mov_b64_e32 v[48:49], 0
	v_mov_b64_e32 v[58:59], 0
	v_mov_b64_e32 v[60:61], 0
	v_mov_b64_e32 v[62:63], 0
	v_mov_b64_e32 v[64:65], 0
	v_mov_b64_e32 v[74:75], 0
	v_mov_b64_e32 v[76:77], 0
	v_mov_b64_e32 v[78:79], 0
	v_mov_b64_e32 v[80:81], 0
	v_mov_b64_e32 v[90:91], 0
	v_mov_b64_e32 v[92:93], 0
	v_mov_b64_e32 v[94:95], 0
	v_mov_b64_e32 v[96:97], 0
	v_mov_b64_e32 v[98:99], 0
	v_mov_b64_e32 v[100:101], 0
	v_mov_b64_e32 v[102:103], 0
	v_mov_b64_e32 v[104:105], 0
	v_mov_b64_e32 v[114:115], 0
	v_mov_b64_e32 v[116:117], 0
	v_mov_b64_e32 v[118:119], 0
	v_mov_b64_e32 v[120:121], 0
	v_mov_b64_e32 v[130:131], 0
	v_mov_b64_e32 v[132:133], 0
	v_mov_b64_e32 v[134:135], 0
	v_mov_b64_e32 v[136:137], 0
	v_mov_b64_e32 v[146:147], 0
	v_mov_b64_e32 v[148:149], 0
	v_mov_b64_e32 v[150:151], 0
	v_mov_b64_e32 v[152:153], 0
	v_mov_b64_e32 v[106:107], 0
	v_mov_b64_e32 v[108:109], 0
	v_mov_b64_e32 v[110:111], 0
	v_mov_b64_e32 v[112:113], 0
	v_mov_b64_e32 v[122:123], 0
	v_mov_b64_e32 v[124:125], 0
	v_mov_b64_e32 v[126:127], 0
	v_mov_b64_e32 v[128:129], 0
	v_mov_b64_e32 v[138:139], 0
	v_mov_b64_e32 v[140:141], 0
	v_mov_b64_e32 v[142:143], 0
	v_mov_b64_e32 v[144:145], 0
	v_mov_b64_e32 v[154:155], 0
	v_mov_b64_e32 v[156:157], 0
	v_mov_b64_e32 v[158:159], 0
	v_mov_b64_e32 v[160:161], 0
	v_mov_b64_e32 v[86:87], 0
	v_mov_b64_e32 v[88:89], 0
	v_mov_b64_e32 v[82:83], 0
	v_mov_b64_e32 v[84:85], 0
	v_mov_b64_e32 v[70:71], 0
	v_mov_b64_e32 v[72:73], 0
	v_mov_b64_e32 v[66:67], 0
	v_mov_b64_e32 v[68:69], 0
	v_mov_b64_e32 v[54:55], 0
	v_mov_b64_e32 v[56:57], 0
	v_mov_b64_e32 v[50:51], 0
	v_mov_b64_e32 v[52:53], 0
	v_mov_b64_e32 v[38:39], 0
	v_mov_b64_e32 v[40:41], 0
	v_mov_b64_e32 v[34:35], 0
	v_mov_b64_e32 v[36:37], 0
	.p2align	6

;     __device__ __forceinline__ void mid(f32x4 (&acc)[2][2][4][2], const Unit& u, int wr, int wc, int fr, int fq) const {
; #pragma unroll
;         for (int ai = 0; ai < 2; ++ai)
; #pragma unroll
;             for (int mp = 0; mp < 2; ++mp) {
;                 uint2 ga[2][2], gm[2][2];
; #pragma unroll
;                 for (int mm = 0; mm < 2; ++mm)
; #pragma unroll
;                     for (int bj = 0; bj < 2; ++bj) { const size_t o = (size_t)(u.pm * BM + wr * 64 + fr + ai * HALF + (2 * mp + mm) * 16) * 2048 + u.pn * BM + wc * 64 + bj * 32 + 8 * fq;
;                         ga[mm][bj] = *(const uint2*)(gate + o); gm[mm][bj] = *(const uint2*)(gate + o + 1024); }
; #pragma unroll
;                 for (int mm = 0; mm < 2; ++mm)
; #pragma unroll
;                     for (int bj = 0; bj < 2; ++bj) { f32x4 a0, a1, m0, m1; ub4(ga[mm][bj].x, a0); ub4(ga[mm][bj].y, a1); ub4(gm[mm][bj].x, m0); ub4(gm[mm][bj].y, m1);
; #pragma unroll
;                         for (int i = 0; i < 4; ++i) { acc[ai][bj][2 * mp + mm][0][i] *= a0[i] * __builtin_amdgcn_rcpf(m0[i]); acc[ai][bj][2 * mp + mm][1][i] *= a1[i] * __builtin_amdgcn_rcpf(m1[i]); } }
;             }
;     }
.LBB0_983:
	global_load_dwordx2 v[178:179], v[148:149], off
	global_load_dwordx2 v[180:181], v[148:149], off offset:1024
	global_load_dwordx2 v[182:183], v[148:149], off offset:1056
	global_load_dwordx2 v[184:185], v[148:149], off offset:32
	global_load_dwordx2 v[186:187], v[150:151], off
	global_load_dwordx2 v[188:189], v[150:151], off offset:1024
	global_load_dwordx2 v[168:169], v[150:151], off offset:1056
	global_load_dwordx2 v[170:171], v[150:151], off offset:32
	s_waitcnt vmcnt(0)
	v_cvt_f32_ubyte0_e32 v190, v178
	v_cvt_f32_ubyte0_e32 v196, v180
	v_cvt_f32_ubyte1_e32 v197, v180
	v_cvt_f32_ubyte2_e32 v198, v180
	v_cvt_f32_ubyte3_e32 v180, v180
	v_cvt_f32_ubyte0_e32 v208, v182
	v_cvt_f32_ubyte1_e32 v209, v182
	v_rcp_iflag_f32_e32 v180, v180
	v_rcp_iflag_f32_e32 v208, v208
	v_rcp_iflag_f32_e32 v196, v196
	v_rcp_iflag_f32_e32 v209, v209
	v_cvt_f32_ubyte1_e32 v191, v178
	v_cvt_f32_ubyte2_e32 v192, v178
	v_cvt_f32_ubyte3_e32 v178, v178
	v_cvt_f32_ubyte0_e32 v202, v184
	v_cvt_f32_ubyte2_e32 v211, v182
	v_cvt_f32_ubyte3_e32 v182, v182
	v_cvt_f32_ubyte1_e32 v203, v184
	v_rcp_iflag_f32_e32 v182, v182
	v_mul_f32_e32 v178, v180, v178
	v_mul_f32_e32 v180, v208, v202
	v_cvt_f32_ubyte0_e32 v199, v181
	v_cvt_f32_ubyte1_e32 v200, v181
	v_cvt_f32_ubyte2_e32 v201, v181
	v_cvt_f32_ubyte3_e32 v181, v181
	v_cvt_f32_ubyte0_e32 v212, v183
	v_rcp_iflag_f32_e32 v198, v198
	v_mul_f32_e32 v190, v196, v190
	v_mul_f32_e32 v196, v209, v203
	v_mul_f32_e32 v118, v118, v180
	v_cvt_f32_ubyte0_e32 v180, v188
	v_rcp_iflag_f32_e32 v200, v200
	v_rcp_iflag_f32_e32 v181, v181
	v_rcp_iflag_f32_e32 v212, v212
	v_mul_f32_e32 v119, v119, v196
	v_rcp_iflag_f32_e32 v196, v180
	v_cvt_f32_ubyte2_e32 v204, v184
	v_cvt_f32_ubyte3_e32 v184, v184
	v_cvt_f32_ubyte1_e32 v213, v183
	v_cvt_f32_ubyte2_e32 v214, v183
	v_cvt_f32_ubyte3_e32 v183, v183
	v_mul_f32_e32 v182, v182, v184
	v_cvt_f32_ubyte0_e32 v193, v179
	v_cvt_f32_ubyte1_e32 v194, v179
	v_cvt_f32_ubyte2_e32 v195, v179
	v_cvt_f32_ubyte3_e32 v179, v179
	v_cvt_f32_ubyte0_e32 v205, v185
	v_rcp_iflag_f32_e32 v183, v183
	v_mul_f32_e32 v192, v198, v192
	v_mul_f32_e32 v121, v121, v182
	v_cvt_f32_ubyte0_e32 v182, v186
	v_rcp_iflag_f32_e32 v199, v199
	v_mul_f32_e32 v194, v200, v194
	v_mul_f32_e32 v179, v181, v179
	v_mul_f32_e32 v181, v212, v205
	v_mul_f32_e32 v128, v128, v192
	v_cvt_f32_ubyte1_e32 v192, v188
	v_mul_f32_e32 v182, v196, v182
	v_rcp_iflag_f32_e32 v201, v201
	v_mul_f32_e32 v123, v123, v194
	v_mul_f32_e32 v129, v129, v178
	v_mul_f32_e32 v125, v125, v179
	v_mul_f32_e32 v114, v114, v181
	global_load_dwordx2 v[178:179], v[152:153], off
	global_load_dwordx2 v[180:181], v[152:153], off offset:1024
	v_cvt_f32_ubyte0_e32 v194, v189
	v_mul_f32_e32 v110, v110, v182
	v_rcp_iflag_f32_e32 v182, v192
	v_cvt_f32_ubyte1_e32 v206, v185
	v_cvt_f32_ubyte2_e32 v207, v185
	v_cvt_f32_ubyte3_e32 v185, v185
	v_rcp_iflag_f32_e32 v194, v194
	v_mul_f32_e32 v183, v183, v185
	v_mul_f32_e32 v193, v199, v193
	v_mul_f32_e32 v117, v117, v183
	v_cvt_f32_ubyte1_e32 v183, v186
	v_mul_f32_e32 v195, v201, v195
	v_mul_f32_e32 v122, v122, v193
	v_cvt_f32_ubyte2_e32 v184, v186
	v_cvt_f32_ubyte3_e32 v185, v186
	v_cvt_f32_ubyte0_e32 v186, v187
	v_cvt_f32_ubyte2_e32 v193, v188
	v_mul_f32_e32 v182, v182, v183
	v_rcp_iflag_f32_e32 v197, v197
	v_rcp_iflag_f32_e32 v213, v213
	v_mul_f32_e32 v124, v124, v195
	v_cvt_f32_ubyte1_e32 v195, v189
	v_mul_f32_e32 v186, v194, v186
	v_mul_f32_e32 v111, v111, v182
	v_rcp_iflag_f32_e32 v182, v193
	v_mul_f32_e32 v106, v106, v186
	v_rcp_iflag_f32_e32 v186, v195
	v_mul_f32_e32 v191, v197, v191
	v_mul_f32_e32 v197, v213, v206
	v_mul_f32_e32 v126, v126, v190
	v_cvt_f32_ubyte1_e32 v190, v187
	v_cvt_f32_ubyte3_e32 v188, v188
	v_mul_f32_e32 v182, v182, v184
	v_mul_f32_e32 v115, v115, v197
	v_cvt_f32_ubyte2_e32 v197, v189
	v_cvt_f32_ubyte3_e32 v189, v189
	v_mul_f32_e32 v183, v186, v190
	v_mul_f32_e32 v112, v112, v182
	v_rcp_iflag_f32_e32 v182, v188
	v_mul_f32_e32 v107, v107, v183
	v_rcp_iflag_f32_e32 v183, v197
	v_rcp_iflag_f32_e32 v184, v189
	v_mul_f32_e32 v127, v127, v191
	v_cvt_f32_ubyte2_e32 v191, v187
	v_cvt_f32_ubyte3_e32 v187, v187
	v_mul_f32_e32 v182, v182, v185
	v_mul_f32_e32 v183, v183, v191
	v_mul_f32_e32 v113, v113, v182
	v_mul_f32_e32 v182, v184, v187
	v_mul_f32_e32 v108, v108, v183
	v_mul_f32_e32 v109, v109, v182
	global_load_dwordx2 v[182:183], v[152:153], off offset:1056
	global_load_dwordx2 v[184:185], v[152:153], off offset:32
	v_cvt_f32_ubyte0_e32 v192, v168
	v_cvt_f32_ubyte0_e32 v195, v169
	v_rcp_iflag_f32_e32 v192, v192
	v_rcp_iflag_f32_e32 v195, v195
	v_cvt_f32_ubyte0_e32 v186, v170
	v_cvt_f32_ubyte0_e32 v189, v171
	v_cvt_f32_ubyte1_e32 v193, v168
	v_mul_f32_e32 v186, v192, v186
	v_cvt_f32_ubyte1_e32 v196, v169
	v_mul_f32_e32 v102, v102, v186
	v_rcp_iflag_f32_e32 v186, v193
	v_mul_f32_e32 v189, v195, v189
	v_mul_f32_e32 v98, v98, v189
	v_rcp_iflag_f32_e32 v189, v196
	v_cvt_f32_ubyte1_e32 v187, v170
	v_cvt_f32_ubyte1_e32 v190, v171
	v_cvt_f32_ubyte2_e32 v194, v168
	v_cvt_f32_ubyte3_e32 v168, v168
	v_mul_f32_e32 v186, v186, v187
	v_cvt_f32_ubyte2_e32 v197, v169
	v_cvt_f32_ubyte3_e32 v169, v169
	v_mul_f32_e32 v103, v103, v186
	v_rcp_iflag_f32_e32 v186, v194
	v_mul_f32_e32 v187, v189, v190
	v_rcp_iflag_f32_e32 v168, v168
	v_mul_f32_e32 v99, v99, v187
	v_rcp_iflag_f32_e32 v187, v197
	v_rcp_iflag_f32_e32 v169, v169
	v_cvt_f32_ubyte2_e32 v188, v170
	v_cvt_f32_ubyte3_e32 v170, v170
	v_cvt_f32_ubyte2_e32 v191, v171
	v_cvt_f32_ubyte3_e32 v171, v171
	v_mul_f32_e32 v186, v186, v188
	v_mul_f32_e32 v168, v168, v170
	v_mul_f32_e32 v104, v104, v186
	v_mul_f32_e32 v186, v187, v191
	v_mul_f32_e32 v105, v105, v168
	v_mul_f32_e32 v168, v169, v171
	v_mul_f32_e32 v100, v100, v186
	v_mul_f32_e32 v101, v101, v168
	global_load_dwordx2 v[186:187], v[154:155], off
	global_load_dwordx2 v[188:189], v[154:155], off offset:1024
	global_load_dwordx2 v[168:169], v[154:155], off offset:1056
	global_load_dwordx2 v[170:171], v[154:155], off offset:32
	s_waitcnt vmcnt(0)
;     __device__ __forceinline__ void mid(f32x4 (&acc)[2][2][4][2], const Unit& u, int wr, int wc, int fr, int fq) const {
; #pragma unroll
;         for (int ai = 0; ai < 2; ++ai)
; #pragma unroll
;             for (int mp = 0; mp < 2; ++mp) {
;                 uint2 ga[2][2], gm[2][2];
; #pragma unroll
;                 for (int mm = 0; mm < 2; ++mm)
; #pragma unroll
;                     for (int bj = 0; bj < 2; ++bj) { const size_t o = (size_t)(u.pm * BM + wr * 64 + fr + ai * HALF + (2 * mp + mm) * 16) * 2048 + u.pn * BM + wc * 64 + bj * 32 + 8 * fq;
;                         ga[mm][bj] = *(const uint2*)(gate + o); gm[mm][bj] = *(const uint2*)(gate + o + 1024); }
; #pragma unroll
;                 for (int mm = 0; mm < 2; ++mm)
; #pragma unroll
;                     for (int bj = 0; bj < 2; ++bj) { f32x4 a0, a1, m0, m1; ub4(ga[mm][bj].x, a0); ub4(ga[mm][bj].y, a1); ub4(gm[mm][bj].x, m0); ub4(gm[mm][bj].y, m1);
; #pragma unroll
;                         for (int i = 0; i < 4; ++i) { acc[ai][bj][2 * mp + mm][0][i] *= a0[i] * __builtin_amdgcn_rcpf(m0[i]); acc[ai][bj][2 * mp + mm][1][i] *= a1[i] * __builtin_amdgcn_rcpf(m1[i]); } }
;             }
;     }
	v_cvt_f32_ubyte0_e32 v196, v180
	v_rcp_iflag_f32_e32 v196, v196
	v_cvt_f32_ubyte0_e32 v190, v178
	v_rcp_iflag_f32_e32 v211, v211
	v_rcp_iflag_f32_e32 v214, v214
	v_cvt_f32_ubyte1_e32 v197, v180
	v_mul_f32_e32 v190, v196, v190
	v_mul_f32_e32 v94, v94, v190
	v_rcp_iflag_f32_e32 v190, v197
	v_mul_f32_e32 v198, v211, v204
	v_mul_f32_e32 v199, v214, v207
	v_cvt_f32_ubyte1_e32 v191, v178
	v_mul_f32_e32 v120, v120, v198
	v_mul_f32_e32 v116, v116, v199
	v_cvt_f32_ubyte2_e32 v198, v180
	v_cvt_f32_ubyte0_e32 v199, v181
	v_mul_f32_e32 v190, v190, v191
	v_rcp_iflag_f32_e32 v199, v199
	v_mul_f32_e32 v95, v95, v190
	v_rcp_iflag_f32_e32 v190, v198
	v_cvt_f32_ubyte3_e32 v180, v180
	v_cvt_f32_ubyte1_e32 v200, v181
	v_cvt_f32_ubyte2_e32 v201, v181
	v_cvt_f32_ubyte3_e32 v181, v181
	v_rcp_iflag_f32_e32 v180, v180
	v_cvt_f32_ubyte2_e32 v192, v178
	v_cvt_f32_ubyte0_e32 v193, v179
	v_rcp_iflag_f32_e32 v181, v181
	v_mul_f32_e32 v193, v199, v193
	v_mul_f32_e32 v190, v190, v192
	v_cvt_f32_ubyte3_e32 v178, v178
	v_mul_f32_e32 v90, v90, v193
	v_rcp_iflag_f32_e32 v193, v200
	v_cvt_f32_ubyte1_e32 v194, v179
	v_cvt_f32_ubyte2_e32 v195, v179
	v_cvt_f32_ubyte3_e32 v179, v179
	v_mul_f32_e32 v178, v180, v178
	v_cvt_f32_ubyte0_e32 v192, v182
	v_rcp_iflag_f32_e32 v192, v192
	v_mul_f32_e32 v97, v97, v178
	v_mul_f32_e32 v178, v181, v179
	v_mul_f32_e32 v93, v93, v178
	v_cvt_f32_ubyte0_e32 v178, v184
	v_mul_f32_e32 v191, v193, v194
	v_cvt_f32_ubyte1_e32 v193, v182
	v_mul_f32_e32 v178, v192, v178
	v_mul_f32_e32 v86, v86, v178
	v_rcp_iflag_f32_e32 v178, v193
	v_mul_f32_e32 v91, v91, v191
	v_rcp_iflag_f32_e32 v191, v201
	v_cvt_f32_ubyte1_e32 v179, v184
	v_cvt_f32_ubyte2_e32 v194, v182
	v_mul_f32_e32 v178, v178, v179
	v_mul_f32_e32 v96, v96, v190
	v_mul_f32_e32 v190, v191, v195
	v_cvt_f32_ubyte0_e32 v195, v183
	v_mul_f32_e32 v87, v87, v178
	v_rcp_iflag_f32_e32 v178, v194
	v_rcp_iflag_f32_e32 v195, v195
	v_cvt_f32_ubyte2_e32 v180, v184
	v_cvt_f32_ubyte3_e32 v181, v184
	v_cvt_f32_ubyte0_e32 v184, v185
	v_cvt_f32_ubyte3_e32 v182, v182
	v_mul_f32_e32 v178, v178, v180
	v_cvt_f32_ubyte1_e32 v196, v183
	v_cvt_f32_ubyte2_e32 v197, v183
	v_cvt_f32_ubyte3_e32 v183, v183
	v_mul_f32_e32 v184, v195, v184
	v_mul_f32_e32 v88, v88, v178
	v_rcp_iflag_f32_e32 v178, v182
	v_mul_f32_e32 v82, v82, v184
	v_rcp_iflag_f32_e32 v184, v196
	v_rcp_iflag_f32_e32 v180, v183
	v_mul_f32_e32 v92, v92, v190
	v_cvt_f32_ubyte1_e32 v190, v185
	v_cvt_f32_ubyte2_e32 v191, v185
	v_cvt_f32_ubyte3_e32 v185, v185
	v_mul_f32_e32 v178, v178, v181
	v_mul_f32_e32 v179, v184, v190
	v_mul_f32_e32 v89, v89, v178
	v_mul_f32_e32 v178, v180, v185
	v_cvt_f32_ubyte0_e32 v180, v188
	v_mul_f32_e32 v83, v83, v179
	v_rcp_iflag_f32_e32 v179, v197
	v_rcp_iflag_f32_e32 v196, v180
	v_cvt_f32_ubyte0_e32 v182, v186
	v_cvt_f32_ubyte1_e32 v192, v188
	v_mul_f32_e32 v179, v179, v191
	v_mul_f32_e32 v182, v196, v182
	v_mul_f32_e32 v84, v84, v179
	v_mul_f32_e32 v85, v85, v178
	global_load_dwordx2 v[178:179], v[156:157], off
	global_load_dwordx2 v[180:181], v[156:157], off offset:1024
	v_cvt_f32_ubyte0_e32 v194, v189
	v_mul_f32_e32 v78, v78, v182
	v_rcp_iflag_f32_e32 v182, v192
	v_rcp_iflag_f32_e32 v194, v194
	v_cvt_f32_ubyte1_e32 v183, v186
	v_cvt_f32_ubyte2_e32 v184, v186
	v_cvt_f32_ubyte3_e32 v185, v186
	v_cvt_f32_ubyte0_e32 v186, v187
	v_cvt_f32_ubyte2_e32 v193, v188
	v_mul_f32_e32 v182, v182, v183
	v_cvt_f32_ubyte1_e32 v195, v189
	v_mul_f32_e32 v186, v194, v186
	v_mul_f32_e32 v79, v79, v182
	v_rcp_iflag_f32_e32 v182, v193
	v_mul_f32_e32 v74, v74, v186
	v_rcp_iflag_f32_e32 v186, v195
	v_cvt_f32_ubyte1_e32 v190, v187
	v_cvt_f32_ubyte3_e32 v188, v188
	v_mul_f32_e32 v182, v182, v184
	v_cvt_f32_ubyte2_e32 v197, v189
	v_cvt_f32_ubyte3_e32 v189, v189
	v_mul_f32_e32 v183, v186, v190
	v_mul_f32_e32 v80, v80, v182
	v_rcp_iflag_f32_e32 v182, v188
	v_mul_f32_e32 v75, v75, v183
	v_rcp_iflag_f32_e32 v183, v197
	v_rcp_iflag_f32_e32 v184, v189
	v_cvt_f32_ubyte2_e32 v191, v187
	v_cvt_f32_ubyte3_e32 v187, v187
	v_mul_f32_e32 v182, v182, v185
	v_mul_f32_e32 v183, v183, v191
	v_mul_f32_e32 v81, v81, v182
	v_mul_f32_e32 v182, v184, v187
	v_mul_f32_e32 v76, v76, v183
	v_mul_f32_e32 v77, v77, v182
	global_load_dwordx2 v[182:183], v[156:157], off offset:1056
	global_load_dwordx2 v[184:185], v[156:157], off offset:32
	v_cvt_f32_ubyte0_e32 v192, v168
	v_cvt_f32_ubyte0_e32 v195, v169
	v_rcp_iflag_f32_e32 v192, v192
	v_rcp_iflag_f32_e32 v195, v195
	v_cvt_f32_ubyte0_e32 v186, v170
	v_cvt_f32_ubyte0_e32 v189, v171
	v_cvt_f32_ubyte1_e32 v193, v168
	v_mul_f32_e32 v186, v192, v186
	v_cvt_f32_ubyte1_e32 v196, v169
	v_mul_f32_e32 v70, v70, v186
	v_rcp_iflag_f32_e32 v186, v193
	v_mul_f32_e32 v189, v195, v189
	v_mul_f32_e32 v66, v66, v189
	v_rcp_iflag_f32_e32 v189, v196
	v_cvt_f32_ubyte1_e32 v187, v170
	v_cvt_f32_ubyte1_e32 v190, v171
	v_cvt_f32_ubyte2_e32 v194, v168
	v_cvt_f32_ubyte3_e32 v168, v168
	v_mul_f32_e32 v186, v186, v187
	v_cvt_f32_ubyte2_e32 v197, v169
	v_cvt_f32_ubyte3_e32 v169, v169
	v_mul_f32_e32 v71, v71, v186
	v_rcp_iflag_f32_e32 v186, v194
	v_mul_f32_e32 v187, v189, v190
	v_rcp_iflag_f32_e32 v168, v168
	v_mul_f32_e32 v67, v67, v187
	v_rcp_iflag_f32_e32 v187, v197
	v_rcp_iflag_f32_e32 v169, v169
	v_cvt_f32_ubyte2_e32 v188, v170
	v_cvt_f32_ubyte3_e32 v170, v170
	v_cvt_f32_ubyte2_e32 v191, v171
	v_cvt_f32_ubyte3_e32 v171, v171
	v_mul_f32_e32 v186, v186, v188
	v_mul_f32_e32 v168, v168, v170
	v_mul_f32_e32 v72, v72, v186
	v_mul_f32_e32 v186, v187, v191
	v_mul_f32_e32 v73, v73, v168
	v_mul_f32_e32 v168, v169, v171
	v_mul_f32_e32 v68, v68, v186
	v_mul_f32_e32 v69, v69, v168
	global_load_dwordx2 v[186:187], v[158:159], off
	global_load_dwordx2 v[188:189], v[158:159], off offset:1024
	global_load_dwordx2 v[168:169], v[158:159], off offset:1056
	global_load_dwordx2 v[170:171], v[158:159], off offset:32
	s_waitcnt vmcnt(0)
;     __device__ __forceinline__ void mid(f32x4 (&acc)[2][2][4][2], const Unit& u, int wr, int wc, int fr, int fq) const {
; #pragma unroll
;         for (int ai = 0; ai < 2; ++ai)
; #pragma unroll
;             for (int mp = 0; mp < 2; ++mp) {
;                 uint2 ga[2][2], gm[2][2];
; #pragma unroll
;                 for (int mm = 0; mm < 2; ++mm)
; #pragma unroll
;                     for (int bj = 0; bj < 2; ++bj) { const size_t o = (size_t)(u.pm * BM + wr * 64 + fr + ai * HALF + (2 * mp + mm) * 16) * 2048 + u.pn * BM + wc * 64 + bj * 32 + 8 * fq;
;                         ga[mm][bj] = *(const uint2*)(gate + o); gm[mm][bj] = *(const uint2*)(gate + o + 1024); }
; #pragma unroll
;                 for (int mm = 0; mm < 2; ++mm)
; #pragma unroll
;                     for (int bj = 0; bj < 2; ++bj) { f32x4 a0, a1, m0, m1; ub4(ga[mm][bj].x, a0); ub4(ga[mm][bj].y, a1); ub4(gm[mm][bj].x, m0); ub4(gm[mm][bj].y, m1);
; #pragma unroll
;                         for (int i = 0; i < 4; ++i) { acc[ai][bj][2 * mp + mm][0][i] *= a0[i] * __builtin_amdgcn_rcpf(m0[i]); acc[ai][bj][2 * mp + mm][1][i] *= a1[i] * __builtin_amdgcn_rcpf(m1[i]); } }
;             }
;     }
	v_cvt_f32_ubyte0_e32 v190, v178
	v_cvt_f32_ubyte0_e32 v196, v180
	v_rcp_iflag_f32_e32 v196, v196
	v_cvt_f32_ubyte1_e32 v197, v180
	v_cvt_f32_ubyte1_e32 v191, v178
	v_cvt_f32_ubyte2_e32 v198, v180
	v_mul_f32_e32 v190, v196, v190
	v_mul_f32_e32 v62, v62, v190
	v_rcp_iflag_f32_e32 v190, v197
	v_cvt_f32_ubyte0_e32 v199, v181
	v_rcp_iflag_f32_e32 v199, v199
	v_cvt_f32_ubyte3_e32 v180, v180
	v_mul_f32_e32 v190, v190, v191
	v_mul_f32_e32 v63, v63, v190
	v_rcp_iflag_f32_e32 v190, v198
	v_cvt_f32_ubyte1_e32 v200, v181
	v_cvt_f32_ubyte2_e32 v201, v181
	v_cvt_f32_ubyte3_e32 v181, v181
	v_rcp_iflag_f32_e32 v180, v180
	v_cvt_f32_ubyte2_e32 v192, v178
	v_cvt_f32_ubyte0_e32 v193, v179
	v_rcp_iflag_f32_e32 v181, v181
	v_mul_f32_e32 v193, v199, v193
	v_mul_f32_e32 v190, v190, v192
	v_cvt_f32_ubyte3_e32 v178, v178
	v_mul_f32_e32 v58, v58, v193
	v_rcp_iflag_f32_e32 v193, v200
	v_cvt_f32_ubyte1_e32 v194, v179
	v_cvt_f32_ubyte2_e32 v195, v179
	v_cvt_f32_ubyte3_e32 v179, v179
	v_mul_f32_e32 v178, v180, v178
	v_mul_f32_e32 v65, v65, v178
	v_mul_f32_e32 v178, v181, v179
	v_mul_f32_e32 v61, v61, v178
	v_mul_f32_e32 v191, v193, v194
	v_mul_f32_e32 v59, v59, v191
	v_cvt_f32_ubyte0_e32 v192, v182
	v_rcp_iflag_f32_e32 v192, v192
	v_cvt_f32_ubyte0_e32 v178, v184
	v_cvt_f32_ubyte1_e32 v193, v182
	v_rcp_iflag_f32_e32 v191, v201
	v_mul_f32_e32 v178, v192, v178
	v_mul_f32_e32 v54, v54, v178
	v_rcp_iflag_f32_e32 v178, v193
	v_cvt_f32_ubyte1_e32 v179, v184
	v_cvt_f32_ubyte2_e32 v194, v182
	v_mul_f32_e32 v64, v64, v190
	v_mul_f32_e32 v178, v178, v179
	v_mul_f32_e32 v190, v191, v195
	v_cvt_f32_ubyte0_e32 v195, v183
	v_mul_f32_e32 v55, v55, v178
	v_rcp_iflag_f32_e32 v178, v194
	v_rcp_iflag_f32_e32 v195, v195
	v_cvt_f32_ubyte2_e32 v180, v184
	v_cvt_f32_ubyte3_e32 v181, v184
	v_cvt_f32_ubyte0_e32 v184, v185
	v_cvt_f32_ubyte3_e32 v182, v182
	v_mul_f32_e32 v178, v178, v180
	v_cvt_f32_ubyte1_e32 v196, v183
	v_cvt_f32_ubyte2_e32 v197, v183
	v_cvt_f32_ubyte3_e32 v183, v183
	v_mul_f32_e32 v184, v195, v184
	v_mul_f32_e32 v56, v56, v178
	v_rcp_iflag_f32_e32 v178, v182
	v_mul_f32_e32 v50, v50, v184
	v_rcp_iflag_f32_e32 v184, v196
	v_rcp_iflag_f32_e32 v180, v183
	v_mul_f32_e32 v60, v60, v190
	v_cvt_f32_ubyte1_e32 v190, v185
	v_cvt_f32_ubyte2_e32 v191, v185
	v_cvt_f32_ubyte3_e32 v185, v185
	v_mul_f32_e32 v178, v178, v181
	v_mul_f32_e32 v179, v184, v190
	v_mul_f32_e32 v57, v57, v178
	v_mul_f32_e32 v178, v180, v185
	v_mul_f32_e32 v51, v51, v179
	v_cvt_f32_ubyte0_e32 v180, v188
	v_rcp_iflag_f32_e32 v179, v197
	v_rcp_iflag_f32_e32 v196, v180
	v_cvt_f32_ubyte0_e32 v182, v186
	v_cvt_f32_ubyte1_e32 v192, v188
	v_mul_f32_e32 v179, v179, v191
	v_mul_f32_e32 v182, v196, v182
	v_mul_f32_e32 v52, v52, v179
	v_mul_f32_e32 v53, v53, v178
	global_load_dwordx2 v[178:179], v[160:161], off
	global_load_dwordx2 v[180:181], v[160:161], off offset:1024
	v_cvt_f32_ubyte0_e32 v194, v189
	v_mul_f32_e32 v46, v46, v182
	v_rcp_iflag_f32_e32 v182, v192
	v_rcp_iflag_f32_e32 v194, v194
	v_cvt_f32_ubyte1_e32 v183, v186
	v_cvt_f32_ubyte2_e32 v184, v186
	v_cvt_f32_ubyte3_e32 v185, v186
	v_cvt_f32_ubyte0_e32 v186, v187
	v_cvt_f32_ubyte2_e32 v193, v188
	v_mul_f32_e32 v182, v182, v183
	v_cvt_f32_ubyte1_e32 v195, v189
	v_mul_f32_e32 v186, v194, v186
	v_mul_f32_e32 v47, v47, v182
	v_rcp_iflag_f32_e32 v182, v193
	v_mul_f32_e32 v42, v42, v186
	v_rcp_iflag_f32_e32 v186, v195
	v_cvt_f32_ubyte1_e32 v190, v187
	v_cvt_f32_ubyte3_e32 v188, v188
	v_mul_f32_e32 v182, v182, v184
	v_cvt_f32_ubyte2_e32 v197, v189
	v_cvt_f32_ubyte3_e32 v189, v189
	v_mul_f32_e32 v183, v186, v190
	v_mul_f32_e32 v48, v48, v182
	v_rcp_iflag_f32_e32 v182, v188
	v_mul_f32_e32 v43, v43, v183
	v_rcp_iflag_f32_e32 v183, v197
	v_rcp_iflag_f32_e32 v184, v189
	v_cvt_f32_ubyte2_e32 v191, v187
	v_cvt_f32_ubyte3_e32 v187, v187
	v_mul_f32_e32 v182, v182, v185
	v_mul_f32_e32 v183, v183, v191
	v_mul_f32_e32 v49, v49, v182
	v_mul_f32_e32 v182, v184, v187
	v_mul_f32_e32 v44, v44, v183
	v_mul_f32_e32 v45, v45, v182
	global_load_dwordx2 v[182:183], v[160:161], off offset:1056
	global_load_dwordx2 v[184:185], v[160:161], off offset:32
	v_cvt_f32_ubyte0_e32 v192, v168
	v_cvt_f32_ubyte0_e32 v195, v169
	v_rcp_iflag_f32_e32 v192, v192
	v_rcp_iflag_f32_e32 v195, v195
	v_cvt_f32_ubyte0_e32 v186, v170
	v_cvt_f32_ubyte0_e32 v189, v171
	v_cvt_f32_ubyte1_e32 v193, v168
	v_mul_f32_e32 v186, v192, v186
	v_cvt_f32_ubyte1_e32 v196, v169
	v_mul_f32_e32 v38, v38, v186
	v_rcp_iflag_f32_e32 v186, v193
	v_mul_f32_e32 v189, v195, v189
	v_mul_f32_e32 v34, v34, v189
	v_rcp_iflag_f32_e32 v189, v196
	v_cvt_f32_ubyte1_e32 v187, v170
	v_cvt_f32_ubyte1_e32 v190, v171
	v_cvt_f32_ubyte2_e32 v194, v168
	v_cvt_f32_ubyte3_e32 v168, v168
	v_mul_f32_e32 v186, v186, v187
	v_cvt_f32_ubyte2_e32 v197, v169
	v_cvt_f32_ubyte3_e32 v169, v169
	v_mul_f32_e32 v39, v39, v186
	v_rcp_iflag_f32_e32 v186, v194
	v_mul_f32_e32 v187, v189, v190
	v_rcp_iflag_f32_e32 v168, v168
	v_mul_f32_e32 v35, v35, v187
	v_rcp_iflag_f32_e32 v187, v197
	v_rcp_iflag_f32_e32 v169, v169
	v_cvt_f32_ubyte2_e32 v188, v170
	v_cvt_f32_ubyte3_e32 v170, v170
	v_cvt_f32_ubyte2_e32 v191, v171
	v_cvt_f32_ubyte3_e32 v171, v171
	v_mul_f32_e32 v186, v186, v188
	v_mul_f32_e32 v168, v168, v170
	v_mul_f32_e32 v40, v40, v186
	v_mul_f32_e32 v186, v187, v191
	v_mul_f32_e32 v41, v41, v168
	v_mul_f32_e32 v168, v169, v171
	v_mul_f32_e32 v36, v36, v186
	v_mul_f32_e32 v37, v37, v168
	global_load_dwordx2 v[168:169], v[162:163], off
	global_load_dwordx2 v[170:171], v[162:163], off offset:1024
	global_load_dwordx2 v[186:187], v[162:163], off offset:1056
	global_load_dwordx2 v[188:189], v[162:163], off offset:32
	s_waitcnt vmcnt(0)
;     __device__ __forceinline__ void mid(f32x4 (&acc)[2][2][4][2], const Unit& u, int wr, int wc, int fr, int fq) const {
; #pragma unroll
;         for (int ai = 0; ai < 2; ++ai)
; #pragma unroll
;             for (int mp = 0; mp < 2; ++mp) {
;                 uint2 ga[2][2], gm[2][2];
; #pragma unroll
;                 for (int mm = 0; mm < 2; ++mm)
; #pragma unroll
;                     for (int bj = 0; bj < 2; ++bj) { const size_t o = (size_t)(u.pm * BM + wr * 64 + fr + ai * HALF + (2 * mp + mm) * 16) * 2048 + u.pn * BM + wc * 64 + bj * 32 + 8 * fq;
;                         ga[mm][bj] = *(const uint2*)(gate + o); gm[mm][bj] = *(const uint2*)(gate + o + 1024); }
; #pragma unroll
;                 for (int mm = 0; mm < 2; ++mm)
; #pragma unroll
;                     for (int bj = 0; bj < 2; ++bj) { f32x4 a0, a1, m0, m1; ub4(ga[mm][bj].x, a0); ub4(ga[mm][bj].y, a1); ub4(gm[mm][bj].x, m0); ub4(gm[mm][bj].y, m1);
; #pragma unroll
;                         for (int i = 0; i < 4; ++i) { acc[ai][bj][2 * mp + mm][0][i] *= a0[i] * __builtin_amdgcn_rcpf(m0[i]); acc[ai][bj][2 * mp + mm][1][i] *= a1[i] * __builtin_amdgcn_rcpf(m1[i]); } }
;             }
;     }
	v_cvt_f32_ubyte0_e32 v190, v178
	v_cvt_f32_ubyte0_e32 v196, v180
	v_rcp_iflag_f32_e32 v196, v196
	v_cvt_f32_ubyte0_e32 v199, v181
	v_cvt_f32_ubyte1_e32 v197, v180
	v_rcp_iflag_f32_e32 v199, v199
	v_mul_f32_e32 v190, v196, v190
	v_mul_f32_e32 v30, v30, v190
	v_rcp_iflag_f32_e32 v190, v197
	v_cvt_f32_ubyte0_e32 v193, v179
	v_cvt_f32_ubyte1_e32 v191, v178
	v_cvt_f32_ubyte1_e32 v200, v181
	v_mul_f32_e32 v193, v199, v193
	v_cvt_f32_ubyte2_e32 v198, v180
	v_mul_f32_e32 v26, v26, v193
	v_rcp_iflag_f32_e32 v193, v200
	v_mul_f32_e32 v190, v190, v191
	v_mul_f32_e32 v31, v31, v190
	v_rcp_iflag_f32_e32 v190, v198
	v_cvt_f32_ubyte3_e32 v180, v180
	v_cvt_f32_ubyte1_e32 v194, v179
	v_cvt_f32_ubyte2_e32 v201, v181
	v_cvt_f32_ubyte3_e32 v181, v181
	v_rcp_iflag_f32_e32 v180, v180
	v_cvt_f32_ubyte2_e32 v192, v178
	v_mul_f32_e32 v191, v193, v194
	v_rcp_iflag_f32_e32 v181, v181
	v_mul_f32_e32 v27, v27, v191
	v_rcp_iflag_f32_e32 v191, v201
	v_mul_f32_e32 v190, v190, v192
	v_cvt_f32_ubyte3_e32 v178, v178
	v_cvt_f32_ubyte2_e32 v195, v179
	v_cvt_f32_ubyte3_e32 v179, v179
	v_mul_f32_e32 v178, v180, v178
	v_mul_f32_e32 v33, v33, v178
	v_mul_f32_e32 v178, v181, v179
	v_cvt_f32_ubyte0_e32 v192, v182
	v_rcp_iflag_f32_e32 v192, v192
	v_mul_f32_e32 v32, v32, v190
	v_mul_f32_e32 v190, v191, v195
	v_mul_f32_e32 v29, v29, v178
	v_cvt_f32_ubyte0_e32 v178, v184
	v_cvt_f32_ubyte0_e32 v195, v183
	v_cvt_f32_ubyte1_e32 v193, v182
	v_rcp_iflag_f32_e32 v195, v195
	v_mul_f32_e32 v178, v192, v178
	v_mul_f32_e32 v22, v22, v178
	v_rcp_iflag_f32_e32 v178, v193
	v_cvt_f32_ubyte1_e32 v179, v184
	v_cvt_f32_ubyte2_e32 v180, v184
	v_cvt_f32_ubyte3_e32 v181, v184
	v_cvt_f32_ubyte0_e32 v184, v185
	v_cvt_f32_ubyte1_e32 v196, v183
	v_mul_f32_e32 v184, v195, v184
	v_cvt_f32_ubyte2_e32 v194, v182
	v_mul_f32_e32 v18, v18, v184
	v_rcp_iflag_f32_e32 v184, v196
	v_mul_f32_e32 v178, v178, v179
	v_mul_f32_e32 v23, v23, v178
	v_rcp_iflag_f32_e32 v178, v194
	v_mul_f32_e32 v28, v28, v190
	v_cvt_f32_ubyte1_e32 v190, v185
	v_cvt_f32_ubyte2_e32 v197, v183
	v_mul_f32_e32 v179, v184, v190
	v_cvt_f32_ubyte3_e32 v182, v182
	v_mul_f32_e32 v19, v19, v179
	v_rcp_iflag_f32_e32 v179, v197
	v_mul_f32_e32 v178, v178, v180
	v_cvt_f32_ubyte3_e32 v183, v183
	v_mul_f32_e32 v24, v24, v178
	v_rcp_iflag_f32_e32 v178, v182
	v_rcp_iflag_f32_e32 v180, v183
	v_cvt_f32_ubyte2_e32 v191, v185
	v_mul_f32_e32 v179, v179, v191
	v_cvt_f32_ubyte3_e32 v185, v185
	v_mul_f32_e32 v178, v178, v181
	v_cvt_f32_ubyte0_e32 v184, v170
	v_cvt_f32_ubyte0_e32 v191, v171
	v_rcp_iflag_f32_e32 v184, v184
	v_rcp_iflag_f32_e32 v191, v191
	v_mul_f32_e32 v25, v25, v178
	v_mul_f32_e32 v178, v180, v185
	v_mul_f32_e32 v21, v21, v178
	v_cvt_f32_ubyte0_e32 v178, v168
	v_cvt_f32_ubyte0_e32 v181, v169
	v_cvt_f32_ubyte1_e32 v185, v170
	v_mul_f32_e32 v178, v184, v178
	v_cvt_f32_ubyte1_e32 v192, v171
	v_mul_f32_e32 v14, v14, v178
	v_rcp_iflag_f32_e32 v178, v185
	v_mul_f32_e32 v181, v191, v181
	v_mul_f32_e32 v10, v10, v181
	v_rcp_iflag_f32_e32 v181, v192
	v_cvt_f32_ubyte2_e32 v190, v170
	v_cvt_f32_ubyte3_e32 v170, v170
	v_mul_f32_e32 v20, v20, v179
	v_cvt_f32_ubyte1_e32 v179, v168
	v_cvt_f32_ubyte2_e32 v193, v171
	v_cvt_f32_ubyte3_e32 v171, v171
	v_rcp_iflag_f32_e32 v170, v170
	v_cvt_f32_ubyte1_e32 v182, v169
	v_mul_f32_e32 v178, v178, v179
	v_rcp_iflag_f32_e32 v171, v171
	v_mul_f32_e32 v15, v15, v178
	v_rcp_iflag_f32_e32 v178, v190
	v_mul_f32_e32 v179, v181, v182
	v_cvt_f32_ubyte0_e32 v182, v186
	v_cvt_f32_ubyte2_e32 v180, v168
	v_cvt_f32_ubyte3_e32 v168, v168
	v_mul_f32_e32 v11, v11, v179
	v_rcp_iflag_f32_e32 v179, v193
	v_rcp_iflag_f32_e32 v182, v182
	v_cvt_f32_ubyte2_e32 v183, v169
	v_cvt_f32_ubyte3_e32 v169, v169
	v_mul_f32_e32 v168, v170, v168
	v_mul_f32_e32 v17, v17, v168
	v_mul_f32_e32 v168, v171, v169
	v_mul_f32_e32 v178, v178, v180
	v_mul_f32_e32 v13, v13, v168
	v_cvt_f32_ubyte0_e32 v168, v188
	v_mul_f32_e32 v16, v16, v178
	v_mul_f32_e32 v178, v179, v183
	v_cvt_f32_ubyte1_e32 v183, v186
	v_mul_f32_e32 v168, v182, v168
	v_cvt_f32_ubyte2_e32 v184, v186
	v_cvt_f32_ubyte3_e32 v185, v186
	v_cvt_f32_ubyte0_e32 v186, v187
	v_mul_f32_e32 v6, v6, v168
	v_rcp_iflag_f32_e32 v168, v183
	v_rcp_iflag_f32_e32 v186, v186
	v_cvt_f32_ubyte1_e32 v169, v188
	v_mul_f32_e32 v12, v12, v178
	v_cvt_f32_ubyte0_e32 v178, v189
	v_mul_f32_e32 v168, v168, v169
	v_cvt_f32_ubyte2_e32 v170, v188
	v_cvt_f32_ubyte3_e32 v171, v188
	v_cvt_f32_ubyte1_e32 v188, v187
	v_mul_f32_e32 v178, v186, v178
	v_mul_f32_e32 v7, v7, v168
	v_rcp_iflag_f32_e32 v168, v184
	v_mul_f32_e32 v2, v2, v178
	v_rcp_iflag_f32_e32 v178, v188
	v_cvt_f32_ubyte1_e32 v179, v189
	v_mul_f32_e32 v168, v168, v170
	v_cvt_f32_ubyte2_e32 v180, v189
	v_cvt_f32_ubyte3_e32 v181, v189
	v_cvt_f32_ubyte2_e32 v189, v187
	v_cvt_f32_ubyte3_e32 v187, v187
	v_mul_f32_e32 v169, v178, v179
	v_mul_f32_e32 v8, v8, v168
	v_rcp_iflag_f32_e32 v168, v185
	v_mul_f32_e32 v3, v3, v169
	v_rcp_iflag_f32_e32 v169, v189
	v_rcp_iflag_f32_e32 v170, v187
	v_mul_f32_e32 v168, v168, v171
	v_mul_f32_e32 v9, v9, v168
	v_mul_f32_e32 v169, v169, v180
	v_mul_f32_e32 v168, v170, v181
	v_mul_f32_e32 v4, v4, v169
	v_mul_f32_e32 v5, v5, v168
	.p2align	6

; #define PG8_BAR __builtin_amdgcn_s_barrier()
; template <class Epi, class Sched, bool ALIGN_EPI = false, bool SP2 = false>
; __device__ __forceinline__ void gemm_phase(PG8_LAS unsigned char* lds, const Gemm g, const Sched& S, const Epi& E) {
;     ...
; #pragma unroll
;         for (int a = 0; a < 2; ++a)
; #pragma unroll
;             for (int b = 0; b < 2; ++b)
; #pragma unroll
;                 for (int m = 0; m < 4; ++m)
; #pragma unroll
;                     for (int n = 0; n < 2; ++n) acc[a][b][m][n] = (f32x4){0.f, 0.f, 0.f, 0.f};
;         cur = nxt; cA = nA; cB = nB; ++ui;
;         if constexpr (ALIGN_EPI) { if (wr == 1) PG8_BAR; }
.Lzk_3:
	s_add_u32 s56, s56, 0x80
	s_addc_u32 s57, s57, 0
	s_add_u32 s93, s58, 0x100
	s_addc_u32 s94, s59, 0
	s_mov_b32 s58, 0
	v_mov_b64_e32 v[6:7], 0
	v_mov_b64_e32 v[8:9], 0
	v_mov_b64_e32 v[14:15], 0
	v_mov_b64_e32 v[16:17], 0
	v_mov_b64_e32 v[26:27], 0
	v_mov_b64_e32 v[28:29], 0
	v_mov_b64_e32 v[30:31], 0
	v_mov_b64_e32 v[32:33], 0
	v_mov_b64_e32 v[42:43], 0
	v_mov_b64_e32 v[44:45], 0
	v_mov_b64_e32 v[46:47], 0
	v_mov_b64_e32 v[48:49], 0
	v_mov_b64_e32 v[86:87], 0
	v_mov_b64_e32 v[88:89], 0
	v_mov_b64_e32 v[82:83], 0
	v_mov_b64_e32 v[84:85], 0
	v_mov_b64_e32 v[78:79], 0
	v_mov_b64_e32 v[80:81], 0
	v_mov_b64_e32 v[74:75], 0
	v_mov_b64_e32 v[76:77], 0
	v_mov_b64_e32 v[94:95], 0
	v_mov_b64_e32 v[96:97], 0
	v_mov_b64_e32 v[90:91], 0
	v_mov_b64_e32 v[92:93], 0
	v_mov_b64_e32 v[54:55], 0
	v_mov_b64_e32 v[56:57], 0
	v_mov_b64_e32 v[50:51], 0
	v_mov_b64_e32 v[52:53], 0
	v_mov_b64_e32 v[114:115], 0
	v_mov_b64_e32 v[116:117], 0
	v_mov_b64_e32 v[118:119], 0
	v_mov_b64_e32 v[120:121], 0
	v_mov_b64_e32 v[102:103], 0
	v_mov_b64_e32 v[104:105], 0
	v_mov_b64_e32 v[98:99], 0
	v_mov_b64_e32 v[100:101], 0
	v_mov_b64_e32 v[110:111], 0
	v_mov_b64_e32 v[112:113], 0
	v_mov_b64_e32 v[106:107], 0
	v_mov_b64_e32 v[108:109], 0
	v_mov_b64_e32 v[62:63], 0
	v_mov_b64_e32 v[64:65], 0
	v_mov_b64_e32 v[58:59], 0
	v_mov_b64_e32 v[60:61], 0
	v_mov_b64_e32 v[122:123], 0
	v_mov_b64_e32 v[124:125], 0
	v_mov_b64_e32 v[126:127], 0
	v_mov_b64_e32 v[128:129], 0
	v_mov_b64_e32 v[66:67], 0
	v_mov_b64_e32 v[68:69], 0
	v_mov_b64_e32 v[70:71], 0
	v_mov_b64_e32 v[72:73], 0
	v_mov_b64_e32 v[38:39], 0
	v_mov_b64_e32 v[40:41], 0
	v_mov_b64_e32 v[34:35], 0
	v_mov_b64_e32 v[36:37], 0
	v_mov_b64_e32 v[22:23], 0
	v_mov_b64_e32 v[24:25], 0
	v_mov_b64_e32 v[18:19], 0
	v_mov_b64_e32 v[20:21], 0
	v_mov_b64_e32 v[10:11], 0
	v_mov_b64_e32 v[12:13], 0
	v_mov_b64_e32 v[2:3], 0
	v_mov_b64_e32 v[4:5], 0
	.p2align	6

; #define PG8_BAR __builtin_amdgcn_s_barrier()
; template <class Epi, class Sched, bool ALIGN_EPI = false, bool SP2 = false>
; __device__ __forceinline__ void gemm_phase(PG8_LAS unsigned char* lds, const Gemm g, const Sched& S, const Epi& E) {
;     ...
; #pragma unroll
;         for (int a = 0; a < 2; ++a)
; #pragma unroll
;             for (int b = 0; b < 2; ++b)
; #pragma unroll
;                 for (int m = 0; m < 4; ++m)
; #pragma unroll
;                     for (int n = 0; n < 2; ++n) acc[a][b][m][n] = (f32x4){0.f, 0.f, 0.f, 0.f};
;         cur = nxt; cA = nA; cB = nB; ++ui;
;         if constexpr (ALIGN_EPI) { if (wr == 1) PG8_BAR; }
.Lzk_4:
	s_add_u32 s30, s30, 0x80
	s_addc_u32 s31, s31, 0
	s_add_u32 s58, s34, 0x100
	s_addc_u32 s59, s35, 0
	s_mov_b32 s34, 0
	v_mov_b64_e32 v[6:7], 0
	v_mov_b64_e32 v[8:9], 0
	v_mov_b64_e32 v[14:15], 0
	v_mov_b64_e32 v[16:17], 0
	v_mov_b64_e32 v[26:27], 0
	v_mov_b64_e32 v[28:29], 0
	v_mov_b64_e32 v[30:31], 0
	v_mov_b64_e32 v[32:33], 0
	v_mov_b64_e32 v[42:43], 0
	v_mov_b64_e32 v[44:45], 0
	v_mov_b64_e32 v[46:47], 0
	v_mov_b64_e32 v[48:49], 0
	v_mov_b64_e32 v[58:59], 0
	v_mov_b64_e32 v[60:61], 0
	v_mov_b64_e32 v[62:63], 0
	v_mov_b64_e32 v[64:65], 0
	v_mov_b64_e32 v[66:67], 0
	v_mov_b64_e32 v[68:69], 0
	v_mov_b64_e32 v[70:71], 0
	v_mov_b64_e32 v[72:73], 0
	v_mov_b64_e32 v[82:83], 0
	v_mov_b64_e32 v[84:85], 0
	v_mov_b64_e32 v[86:87], 0
	v_mov_b64_e32 v[88:89], 0
	v_mov_b64_e32 v[98:99], 0
	v_mov_b64_e32 v[100:101], 0
	v_mov_b64_e32 v[102:103], 0
	v_mov_b64_e32 v[104:105], 0
	v_mov_b64_e32 v[114:115], 0
	v_mov_b64_e32 v[116:117], 0
	v_mov_b64_e32 v[118:119], 0
	v_mov_b64_e32 v[120:121], 0
	v_mov_b64_e32 v[74:75], 0
	v_mov_b64_e32 v[76:77], 0
	v_mov_b64_e32 v[78:79], 0
	v_mov_b64_e32 v[80:81], 0
	v_mov_b64_e32 v[90:91], 0
	v_mov_b64_e32 v[92:93], 0
	v_mov_b64_e32 v[94:95], 0
	v_mov_b64_e32 v[96:97], 0
	v_mov_b64_e32 v[106:107], 0
	v_mov_b64_e32 v[108:109], 0
	v_mov_b64_e32 v[110:111], 0
	v_mov_b64_e32 v[112:113], 0
	v_mov_b64_e32 v[122:123], 0
	v_mov_b64_e32 v[124:125], 0
	v_mov_b64_e32 v[126:127], 0
	v_mov_b64_e32 v[128:129], 0
	v_mov_b64_e32 v[54:55], 0
	v_mov_b64_e32 v[56:57], 0
	v_mov_b64_e32 v[50:51], 0
	v_mov_b64_e32 v[52:53], 0
	v_mov_b64_e32 v[38:39], 0
	v_mov_b64_e32 v[40:41], 0
	v_mov_b64_e32 v[34:35], 0
	v_mov_b64_e32 v[36:37], 0
	v_mov_b64_e32 v[22:23], 0
	v_mov_b64_e32 v[24:25], 0
	v_mov_b64_e32 v[18:19], 0
	v_mov_b64_e32 v[20:21], 0
	v_mov_b64_e32 v[10:11], 0
	v_mov_b64_e32 v[12:13], 0
	v_mov_b64_e32 v[2:3], 0
	v_mov_b64_e32 v[4:5], 0
	.p2align	6

; #define PG8_BAR __builtin_amdgcn_s_barrier()
; template <class Epi, class Sched, bool ALIGN_EPI = false, bool SP2 = false>
; __device__ __forceinline__ void gemm_phase(PG8_LAS unsigned char* lds, const Gemm g, const Sched& S, const Epi& E) {
;     ...
; #pragma unroll
;         for (int a = 0; a < 2; ++a)
; #pragma unroll
;             for (int b = 0; b < 2; ++b)
; #pragma unroll
;                 for (int m = 0; m < 4; ++m)
; #pragma unroll
;                     for (int n = 0; n < 2; ++n) acc[a][b][m][n] = (f32x4){0.f, 0.f, 0.f, 0.f};
;         cur = nxt; cA = nA; cB = nB; ++ui;
;         if constexpr (ALIGN_EPI) { if (wr == 1) PG8_BAR; }
.Lzk_6:
	s_add_u32 s46, s46, 0x80
	s_addc_u32 s47, s47, 0
	s_add_u32 s80, s48, 0x100
	s_addc_u32 s81, s49, 0
	s_mov_b32 s48, 0
	v_mov_b64_e32 v[42:43], 0
	v_mov_b64_e32 v[44:45], 0
	v_mov_b64_e32 v[46:47], 0
	v_mov_b64_e32 v[48:49], 0
	v_mov_b64_e32 v[58:59], 0
	v_mov_b64_e32 v[60:61], 0
	v_mov_b64_e32 v[62:63], 0
	v_mov_b64_e32 v[64:65], 0
	v_mov_b64_e32 v[74:75], 0
	v_mov_b64_e32 v[76:77], 0
	v_mov_b64_e32 v[78:79], 0
	v_mov_b64_e32 v[80:81], 0
	v_mov_b64_e32 v[90:91], 0
	v_mov_b64_e32 v[92:93], 0
	v_mov_b64_e32 v[94:95], 0
	v_mov_b64_e32 v[96:97], 0
	v_mov_b64_e32 v[98:99], 0
	v_mov_b64_e32 v[100:101], 0
	v_mov_b64_e32 v[102:103], 0
	v_mov_b64_e32 v[104:105], 0
	v_mov_b64_e32 v[114:115], 0
	v_mov_b64_e32 v[116:117], 0
	v_mov_b64_e32 v[118:119], 0
	v_mov_b64_e32 v[120:121], 0
	v_mov_b64_e32 v[130:131], 0
	v_mov_b64_e32 v[132:133], 0
	v_mov_b64_e32 v[134:135], 0
	v_mov_b64_e32 v[136:137], 0
	v_mov_b64_e32 v[146:147], 0
	v_mov_b64_e32 v[148:149], 0
	v_mov_b64_e32 v[150:151], 0
	v_mov_b64_e32 v[152:153], 0
	v_mov_b64_e32 v[106:107], 0
	v_mov_b64_e32 v[108:109], 0
	v_mov_b64_e32 v[110:111], 0
	v_mov_b64_e32 v[112:113], 0
	v_mov_b64_e32 v[122:123], 0
	v_mov_b64_e32 v[124:125], 0
	v_mov_b64_e32 v[126:127], 0
	v_mov_b64_e32 v[128:129], 0
	v_mov_b64_e32 v[138:139], 0
	v_mov_b64_e32 v[140:141], 0
	v_mov_b64_e32 v[142:143], 0
	v_mov_b64_e32 v[144:145], 0
	v_mov_b64_e32 v[154:155], 0
	v_mov_b64_e32 v[156:157], 0
	v_mov_b64_e32 v[158:159], 0
	v_mov_b64_e32 v[160:161], 0
	v_mov_b64_e32 v[86:87], 0
	v_mov_b64_e32 v[88:89], 0
	v_mov_b64_e32 v[82:83], 0
	v_mov_b64_e32 v[84:85], 0
	v_mov_b64_e32 v[70:71], 0
	v_mov_b64_e32 v[72:73], 0
	v_mov_b64_e32 v[66:67], 0
	v_mov_b64_e32 v[68:69], 0
	v_mov_b64_e32 v[54:55], 0
	v_mov_b64_e32 v[56:57], 0
	v_mov_b64_e32 v[50:51], 0
	v_mov_b64_e32 v[52:53], 0
	v_mov_b64_e32 v[38:39], 0
	v_mov_b64_e32 v[40:41], 0
	v_mov_b64_e32 v[34:35], 0
	v_mov_b64_e32 v[36:37], 0
	.p2align	6

; #define PG8_BAR __builtin_amdgcn_s_barrier()
; template <class Epi, class Sched, bool ALIGN_EPI = false, bool SP2 = false>
; __device__ __forceinline__ void gemm_phase(PG8_LAS unsigned char* lds, const Gemm g, const Sched& S, const Epi& E) {
;     ...
; #pragma unroll
;         for (int a = 0; a < 2; ++a)
; #pragma unroll
;             for (int b = 0; b < 2; ++b)
; #pragma unroll
;                 for (int m = 0; m < 4; ++m)
; #pragma unroll
;                     for (int n = 0; n < 2; ++n) acc[a][b][m][n] = (f32x4){0.f, 0.f, 0.f, 0.f};
;         cur = nxt; cA = nA; cB = nB; ++ui;
;         if constexpr (ALIGN_EPI) { if (wr == 1) PG8_BAR; }
.Lzk_7:
	s_add_u32 s2, s80, 0x80
	s_addc_u32 s3, s81, 0
	s_add_u32 s57, s78, 0x100
	s_addc_u32 s82, s79, 0
	s_mov_b32 s78, 0
	v_mov_b64_e32 v[40:41], 0
	v_mov_b64_e32 v[42:43], 0
	v_mov_b64_e32 v[44:45], 0
	v_mov_b64_e32 v[46:47], 0
	v_mov_b64_e32 v[56:57], 0
	v_mov_b64_e32 v[58:59], 0
	v_mov_b64_e32 v[60:61], 0
	v_mov_b64_e32 v[62:63], 0
	v_mov_b64_e32 v[72:73], 0
	v_mov_b64_e32 v[74:75], 0
	v_mov_b64_e32 v[76:77], 0
	v_mov_b64_e32 v[78:79], 0
	v_mov_b64_e32 v[88:89], 0
	v_mov_b64_e32 v[90:91], 0
	v_mov_b64_e32 v[92:93], 0
	v_mov_b64_e32 v[94:95], 0
	v_mov_b64_e32 v[96:97], 0
	v_mov_b64_e32 v[98:99], 0
	v_mov_b64_e32 v[100:101], 0
	v_mov_b64_e32 v[102:103], 0
	v_mov_b64_e32 v[120:121], 0
	v_mov_b64_e32 v[122:123], 0
	v_mov_b64_e32 v[124:125], 0
	v_mov_b64_e32 v[126:127], 0
	v_mov_b64_e32 v[128:129], 0
	v_mov_b64_e32 v[130:131], 0
	v_mov_b64_e32 v[132:133], 0
	v_mov_b64_e32 v[134:135], 0
	v_mov_b64_e32 v[144:145], 0
	v_mov_b64_e32 v[146:147], 0
	v_mov_b64_e32 v[148:149], 0
	v_mov_b64_e32 v[150:151], 0
	v_mov_b64_e32 v[112:113], 0
	v_mov_b64_e32 v[114:115], 0
	v_mov_b64_e32 v[116:117], 0
	v_mov_b64_e32 v[118:119], 0
	v_mov_b64_e32 v[104:105], 0
	v_mov_b64_e32 v[106:107], 0
	v_mov_b64_e32 v[108:109], 0
	v_mov_b64_e32 v[110:111], 0
	v_mov_b64_e32 v[136:137], 0
	v_mov_b64_e32 v[138:139], 0
	v_mov_b64_e32 v[140:141], 0
	v_mov_b64_e32 v[142:143], 0
	v_mov_b64_e32 v[160:161], 0
	v_mov_b64_e32 v[162:163], 0
	v_mov_b64_e32 v[164:165], 0
	v_mov_b64_e32 v[166:167], 0
	v_mov_b64_e32 v[84:85], 0
	v_mov_b64_e32 v[86:87], 0
	v_mov_b64_e32 v[80:81], 0
	v_mov_b64_e32 v[82:83], 0
	v_mov_b64_e32 v[68:69], 0
	v_mov_b64_e32 v[70:71], 0
	v_mov_b64_e32 v[64:65], 0
	v_mov_b64_e32 v[66:67], 0
	v_mov_b64_e32 v[52:53], 0
	v_mov_b64_e32 v[54:55], 0
	v_mov_b64_e32 v[48:49], 0
	v_mov_b64_e32 v[50:51], 0
	v_mov_b64_e32 v[36:37], 0
	v_mov_b64_e32 v[38:39], 0
	v_mov_b64_e32 v[32:33], 0
	v_mov_b64_e32 v[34:35], 0
	.p2align	6
